# speedup vs baseline: 1.0015x; 1.0015x over previous
_Z14moe_persistent8GemmArgs:
	s_load_dwordx8 s[24:31], s[0:1], 0x0
	s_load_dwordx2 s[4:5], s[0:1], 0x20
	s_load_dwordx16 s[8:23], s[0:1], 0x70
	v_mov_b32_e32 v1, 0
	v_mov_b32_e32 v245, 0
	v_cmp_eq_u32_e64 s[6:7], 0, v0
	s_waitcnt lgkmcnt(0)
	v_writelane_b32 v244, s4, 0
	s_nop 1
	v_writelane_b32 v244, s5, 1
	s_and_saveexec_b64 s[4:5], s[6:7]
	s_cbranch_execz .LBB2_4
	s_load_dwordx2 s[44:45], s[0:1], 0x28
	v_mov_b32_e32 v2, 0
	s_and_b32 s99, s2, 7
	s_lshl_b32 s94, s99, 2
	s_add_u32 s94, s10, s94
	s_addc_u32 s95, s11, 0
	v_mov_b32_e32 v11, 1
	global_atomic_add v11, v2, v11, s[94:95] sc0
	s_mov_b64 s[34:35], exec
	s_waitcnt lgkmcnt(0)
	s_load_dwordx8 s[36:43], s[44:45], 0x0
	s_waitcnt lgkmcnt(0)
	s_add_i32 s3, s36, 0xff
	s_add_i32 s33, s37, 0xff
	s_add_i32 s44, s38, 0xff
	s_add_i32 s45, s39, 0xff
	s_ashr_i32 s33, s33, 8
	s_ashr_i32 s3, s3, 8
	s_ashr_i32 s47, s45, 8
	s_mul_i32 s48, s3, 0x2a8
	s_add_i32 s49, s33, s3
	s_ashr_i32 s44, s44, 8
	v_mov_b32_e32 v6, s3
	s_add_i32 s3, 0, 0x20820
	s_add_i32 s51, s44, s49
	v_mov_b32_e32 v7, s33
	v_mov_b32_e32 v8, s44
	v_mov_b32_e32 v9, s47
	v_mov_b32_e32 v1, s3
	s_add_i32 s3, 0, 0x20840
	ds_write_b128 v1, v[6:9]
	v_mov_b32_e32 v4, s49
	v_mov_b32_e32 v5, s51
	v_mov_b32_e32 v3, v6
	v_mov_b32_e32 v1, s3
	ds_write_b128 v1, v[2:5]
	v_mov_b32_e32 v4, s36
	s_add_i32 s3, 0, 0x20860
	s_add_i32 s36, s40, 0xff
	s_mul_i32 s50, s33, 0x2a8
	v_mov_b32_e32 v5, s37
	v_mov_b32_e32 v6, s38
	v_mov_b32_e32 v7, s39
	v_mov_b32_e32 v1, s3
	s_add_i32 s3, s47, s51
	s_mul_i32 s33, s47, 0x2a8
	s_add_i32 s37, s41, 0xff
	s_ashr_i32 s36, s36, 8
	s_add_i32 s47, s42, 0xff
	s_add_i32 s51, s43, 0xff
	s_mul_i32 s52, s44, 0x2a8
	ds_write_b128 v1, v[4:7]
	s_ashr_i32 s37, s37, 8
	s_add_i32 s38, s36, s3
	s_mul_i32 s44, s36, 0x2a8
	s_ashr_i32 s51, s51, 8
	s_ashr_i32 s47, s47, 8
	v_mov_b32_e32 v4, s36
	s_add_i32 s36, 0, 0x20830
	s_add_i32 s39, s37, s38
	v_mov_b32_e32 v5, s37
	v_mov_b32_e32 v6, s47
	v_mov_b32_e32 v7, s51
	v_mov_b32_e32 v1, s36
	s_add_i32 s53, s47, s39
	ds_write_b128 v1, v[4:7]
	v_mov_b32_e32 v4, s3
	s_add_i32 s3, 0, 0x20850
	s_mul_i32 s49, s37, 0x2a8
	s_mul_i32 s54, s47, 0x2a8
	v_mov_b32_e32 v5, s38
	v_mov_b32_e32 v6, s39
	v_mov_b32_e32 v7, s53
	v_mov_b32_e32 v1, s3
	s_add_i32 s3, 0, 0x20870
	ds_write_b128 v1, v[4:7]
	v_mov_b32_e32 v1, s3
	s_add_i32 s3, s50, s52
	s_add_i32 s36, s33, s44
	s_add_i32 s37, s49, s54
	s_add_i32 s3, s48, s3
	s_add_i32 s36, s36, s37
	s_add_i32 s3, s3, s36
	s_and_b32 s99, s2, 7
	s_lshl_b32 s36, s2, 5
	s_and_b32 s36, s36, 0xe0
	s_lshr_b32 s2, s2, 3
	v_mov_b32_e32 v4, s40
	s_mul_i32 s40, s51, 0x2a8
	s_add_i32 s36, s36, s2
	s_add_i32 s46, s48, 0x4b0
	s_add_i32 s3, s3, s40
	s_lshl_b32 s2, s36, 1
	s_addk_i32 s3, 0x2580
	s_or_b32 s2, s2, 1
	s_ashr_i32 s47, s46, 31
	s_addk_i32 s50, 0x4b0
	s_mul_hi_i32 s37, s3, s2
	s_mul_i32 s36, s3, s2
	s_lshl_b64 s[2:3], s[46:47], 9
	s_ashr_i32 s39, s50, 31
	s_add_u32 s38, s50, s46
	v_mov_b32_e32 v5, s41
	v_mov_b32_e32 v6, s42
	v_mov_b32_e32 v7, s43
	s_addc_u32 s39, s39, s47
	ds_write_b128 v1, v[4:7]
	v_mov_b64_e32 v[4:5], s[2:3]
	s_lshl_b64 s[2:3], s[38:39], 9
	v_cmp_ge_i64_e32 vcc, s[36:37], v[4:5]
	v_mov_b64_e32 v[4:5], s[2:3]
	v_cmp_lt_i64_e64 s[2:3], s[36:37], v[4:5]
	s_and_b64 s[2:3], vcc, s[2:3]
	s_addk_i32 s52, 0x4b0
	v_cndmask_b32_e64 v1, 0, 1, s[2:3]
	s_ashr_i32 s2, s52, 31
	s_add_u32 s38, s38, s52
	s_addc_u32 s39, s39, s2
	s_lshl_b64 s[2:3], s[38:39], 9
	v_cmp_ge_i64_e32 vcc, s[36:37], v[4:5]
	v_mov_b64_e32 v[4:5], s[2:3]
	v_cmp_lt_i64_e64 s[2:3], s[36:37], v[4:5]
	s_and_b64 s[2:3], vcc, s[2:3]
	s_and_b64 s[2:3], s[2:3], exec
	v_readfirstlane_b32 s2, v1
	s_cselect_b32 s41, 2, s2
	s_addk_i32 s33, 0x4b0
	s_ashr_i32 s2, s33, 31
	s_add_u32 s38, s38, s33
	s_addc_u32 s39, s39, s2
	s_lshl_b64 s[2:3], s[38:39], 9
	v_cmp_ge_i64_e32 vcc, s[36:37], v[4:5]
	v_mov_b64_e32 v[4:5], s[2:3]
	v_cmp_lt_i64_e64 s[2:3], s[36:37], v[4:5]
	s_and_b64 s[2:3], vcc, s[2:3]
	s_and_b64 s[2:3], s[2:3], exec
	s_cselect_b32 s33, 3, s41
	s_addk_i32 s44, 0x4b0
	s_ashr_i32 s2, s44, 31
	s_add_u32 s38, s38, s44
	s_addc_u32 s39, s39, s2
	s_lshl_b64 s[2:3], s[38:39], 9
	v_cmp_ge_i64_e32 vcc, s[36:37], v[4:5]
	v_mov_b64_e32 v[4:5], s[2:3]
	v_cmp_lt_i64_e64 s[2:3], s[36:37], v[4:5]
	s_and_b64 s[2:3], vcc, s[2:3]
	s_and_b64 s[2:3], s[2:3], exec
	s_cselect_b32 s33, 4, s33
	s_addk_i32 s49, 0x4b0
	s_ashr_i32 s2, s49, 31
	s_add_u32 s38, s38, s49
	s_addc_u32 s39, s39, s2
	s_lshl_b64 s[2:3], s[38:39], 9
	v_cmp_ge_i64_e32 vcc, s[36:37], v[4:5]
	v_mov_b64_e32 v[4:5], s[2:3]
	v_cmp_lt_i64_e64 s[2:3], s[36:37], v[4:5]
	s_and_b64 s[2:3], vcc, s[2:3]
	s_and_b64 s[2:3], s[2:3], exec
	s_cselect_b32 s33, 5, s33
	s_addk_i32 s54, 0x4b0
	s_ashr_i32 s2, s54, 31
	s_add_u32 s38, s38, s54
	s_addc_u32 s39, s39, s2
	s_lshl_b64 s[2:3], s[38:39], 9
	v_cmp_ge_i64_e32 vcc, s[36:37], v[4:5]
	v_mov_b64_e32 v[4:5], s[2:3]
	v_cmp_lt_i64_e64 s[2:3], s[36:37], v[4:5]
	s_and_b64 s[2:3], vcc, s[2:3]
	s_and_b64 s[2:3], s[2:3], exec
	s_cselect_b32 s33, 6, s33
	s_addk_i32 s40, 0x4b0
	s_ashr_i32 s3, s40, 31
	s_add_u32 s2, s38, s40
	s_addc_u32 s3, s39, s3
	s_lshl_b64 s[2:3], s[2:3], 9
	v_cmp_ge_i64_e32 vcc, s[36:37], v[4:5]
	v_mov_b64_e32 v[4:5], s[2:3]
	v_cmp_lt_i64_e64 s[2:3], s[36:37], v[4:5]
	s_and_b64 s[2:3], vcc, s[2:3]
	s_and_b64 s[2:3], s[2:3], exec
	s_cselect_b32 s44, 7, s33
	s_mov_b32 s44, s99
	s_add_i32 s2, 0, 0x20880
	v_mov_b32_e32 v3, v2
	v_mov_b32_e32 v1, s2
	s_add_i32 s2, 0, 0x20808
	ds_write_b64 v1, v[2:3]
	v_mov_b32_e32 v1, s2
	v_mov_b32_e32 v3, s44
	ds_write_b32 v1, v3
	v_mbcnt_lo_u32_b32 v1, s34, 0
	v_mbcnt_hi_u32_b32 v1, s35, v1
	s_mov_b32 s45, 0
	v_cmp_eq_u32_e32 vcc, 0, v1
	s_and_saveexec_b64 s[2:3], vcc
	s_cbranch_execz .LBB2_3
	s_lshl_b64 s[36:37], s[44:45], 2
	s_add_u32 s36, s10, s36
	s_addc_u32 s37, s11, s37
	s_bcnt1_i32_b64 s33, s[34:35]
	v_mov_b32_e32 v3, s33
.LBB2_3:
	s_or_b64 exec, exec, s[2:3]
	s_waitcnt vmcnt(0)
	v_readfirstlane_b32 s2, v11
	s_nop 1
	v_add_u32_e32 v1, s2, v1
